# k-order permuted inside each 32-block (prep + h1 layout) so each lane stores its two hidden tiles as one ds_write_b128; layer 0 rescheduled by hand
# speedup vs baseline: 1.0095x; 1.0040x over previous
.LBB0_77:
	s_or_b64 exec, exec, s[0:1]
	s_and_b32 s10, s2, 3
	s_bfe_u32 s2, s2, 0x30002
	s_lshl_b32 s11, s2, 6
	s_lshl_b32 s0, s3, 20
	s_add_u32 s0, s4, s0
	s_addc_u32 s1, s5, 0
	s_lshl_b32 s4, s2, 17
	s_add_u32 s0, s0, s4
	s_addc_u32 s1, s1, 0
	s_lshl_b32 s4, s10, 9
	s_add_u32 s0, s0, s4
	s_addc_u32 s1, s1, 0
	s_waitcnt lgkmcnt(0)
	v_mov_b32_e32 v3, 0
	s_or_b32 s8, s11, s8
	v_lshrrev_b32_e32 v28, 5, v0
	v_or_b32_e32 v4, s8, v28
	v_mov_b32_e32 v5, v3
	v_lshl_add_u64 v[4:5], v[4:5], 2, s[16:17]
	s_barrier
	global_load_dword v29, v[4:5], off
	v_or_b32_e32 v14, 0x200, v0
	v_lshrrev_b32_e32 v33, 5, v14
	v_or_b32_e32 v2, 0x100, v0
	v_mov_b32_e32 v19, v3
	v_or_b32_e32 v18, s8, v33
	v_lshrrev_b32_e32 v30, 5, v2
	v_lshl_add_u64 v[18:19], v[18:19], 2, s[16:17]
	global_load_dword v34, v[18:19], off
	v_or_b32_e32 v4, s8, v30
	v_mov_b32_e32 v5, v3
	v_lshl_add_u64 v[4:5], v[4:5], 2, s[16:17]
	global_load_dword v31, v[4:5], off
	v_and_b32_e32 v20, 31, v0
	v_lshlrev_b32_e32 v2, 4, v20
	v_lshl_add_u64 v[4:5], s[0:1], 0, v[2:3]
	v_lshlrev_b32_e32 v2, 11, v28
	v_lshl_add_u64 v[6:7], v[4:5], 0, v[2:3]
	global_load_dwordx4 v[6:9], v[6:7], off
	v_mov_b32_e32 v15, v3
	v_lshlrev_b32_e32 v14, 11, v30
	v_lshl_add_u64 v[14:15], v[4:5], 0, v[14:15]
	global_load_dwordx4 v[14:17], v[14:15], off
	ds_read_b128 v[10:13], v3 offset:17408
	s_brev_b32 s11, 34
	v_or_b32_e32 v21, 0x300, v0
	v_lshrrev_b32_e32 v36, 5, v21
	v_mov_b32_e32 v19, v3
	s_waitcnt lgkmcnt(0)
	v_add_f32_e32 v10, v10, v11
	v_add_f32_e32 v10, v10, v12
	v_add_f32_e32 v37, v10, v13
	v_div_scale_f32 v38, s[0:1], v37, v37, s11
	v_rcp_f32_e32 v40, v38
	v_mov_b32_e32 v23, v3
	v_lshlrev_b32_e32 v18, 11, v33
	v_or_b32_e32 v22, s8, v36
	v_lshlrev_b32_e32 v35, 3, v20
	v_mov_b32_e32 v21, v3
	v_lshlrev_b32_e32 v20, 11, v36
	v_lshl_add_u64 v[24:25], v[4:5], 0, v[18:19]
	v_lshl_add_u64 v[22:23], v[22:23], 2, s[16:17]
	v_lshl_add_u64 v[26:27], v[4:5], 0, v[20:21]
	global_load_dwordx4 v[10:13], v[24:25], off
	global_load_dword v41, v[22:23], off
	global_load_dwordx4 v[18:21], v[26:27], off
	v_fma_f32 v22, -v38, v40, 1.0
	v_div_scale_f32 v39, vcc, s11, v37, s11
	v_fmac_f32_e32 v40, v22, v40
	v_mul_f32_e32 v22, v39, v40
	v_fma_f32 v23, -v38, v22, v39
	v_fmac_f32_e32 v22, v23, v40
	v_fma_f32 v23, -v38, v22, v39
	v_div_fmas_f32 v22, v23, v40, v22
	v_div_fixup_f32 v37, v22, v37, s11
	s_mov_b32 s5, 0x800000
	v_mov_b32_e32 v32, 0x42000000
	v_or_b32_e32 v2, 0x10000, v2
	s_mov_b32 s4, 0x39800000
	s_waitcnt vmcnt(7)
	v_mul_f32_e32 v22, v29, v29
	v_mul_f32_e32 v22, v37, v22
	v_max_f32_e32 v22, 0x2b8cbccc, v22
	v_cmp_gt_f32_e32 vcc, s5, v22
	s_waitcnt vmcnt(5)
	v_mul_f32_e32 v23, v31, v31
	v_cndmask_b32_e64 v24, 0, 32, vcc
	v_ldexp_f32 v22, v22, v24
	v_log_f32_e32 v22, v22
	v_mul_f32_e32 v23, v37, v23
	v_max_f32_e32 v23, 0x2b8cbccc, v23
	v_cndmask_b32_e32 v24, 0, v32, vcc
	v_cmp_gt_f32_e64 s[0:1], s5, v23
	v_sub_f32_e32 v22, v22, v24
	v_mul_f32_e32 v22, 0.5, v22
	v_cndmask_b32_e64 v25, 0, 32, s[0:1]
	v_ldexp_f32 v23, v23, v25
	v_rndne_f32_e32 v22, v22
	v_log_f32_e32 v25, v23
	v_cvt_i32_f32_e32 v24, v22
	v_lshl_add_u64 v[22:23], v[4:5], 0, v[2:3]
	v_cndmask_b32_e64 v2, 0, v32, s[0:1]
	v_sub_f32_e32 v25, v25, v2
	v_sub_u32_e32 v2, 0, v24
	v_med3_i32 v2, v2, -1, 3
	v_sub_u32_e32 v2, 0, v2
	v_ldexp_f32 v2, s4, v2
	s_waitcnt vmcnt(4)
	v_pk_mul_f32 v[6:7], v[6:7], v[2:3] op_sel_hi:[1,0]
	v_pk_mul_f32 v[8:9], v[8:9], v[2:3] op_sel_hi:[1,0]
	v_add_u32_e32 v2, s8, v28
	v_cvt_pk_f16_f32 v6, v6, v7
	v_cvt_pk_f16_f32 v7, v8, v9
	v_lshl_add_u64 v[8:9], v[2:3], 2, s[16:17]
	global_load_dword v29, v[8:9], off offset:128
	v_mul_f32_e32 v2, 0.5, v25
	v_rndne_f32_e32 v2, v2
	v_cvt_i32_f32_e32 v2, v2
	s_movk_i32 s0, 0x110
	v_mad_u32_u24 v28, v28, s0, v35
	ds_write_b64 v28, v[6:7]
	v_sub_u32_e32 v2, 0, v2
	v_med3_i32 v2, v2, -1, 3
	v_sub_u32_e32 v2, 0, v2
	v_ldexp_f32 v2, s4, v2
	s_waitcnt vmcnt(4)
	v_pk_mul_f32 v[6:7], v[14:15], v[2:3] op_sel_hi:[1,0]
	v_mul_f32_e32 v8, v34, v34
	v_cvt_pk_f16_f32 v14, v6, v7
	v_pk_mul_f32 v[6:7], v[16:17], v[2:3] op_sel_hi:[1,0]
	v_or_b32_e32 v2, 0x500, v0
	v_lshrrev_b32_e32 v31, 5, v2
	v_lshlrev_b32_e32 v2, 11, v31
	v_lshl_add_u64 v[16:17], v[4:5], 0, v[2:3]
	v_add_u32_e32 v2, s8, v31
	v_cvt_pk_f16_f32 v15, v6, v7
	v_lshl_add_u64 v[6:7], v[2:3], 2, s[16:17]
	v_mul_f32_e32 v2, v37, v8
	v_max_f32_e32 v2, 0x2b8cbccc, v2
	v_cmp_gt_f32_e32 vcc, s5, v2
	global_load_dword v34, v[6:7], off
	s_nop 0
	v_cndmask_b32_e64 v6, 0, 32, vcc
	v_ldexp_f32 v2, v2, v6
	v_log_f32_e32 v2, v2
	global_load_dwordx4 v[6:9], v[22:23], off
	v_mad_u32_u24 v22, v30, s0, v35
	ds_write_b64 v22, v[14:15]
	v_cndmask_b32_e32 v14, 0, v32, vcc
	v_sub_f32_e32 v2, v2, v14
	v_mul_f32_e32 v2, 0.5, v2
	v_rndne_f32_e32 v2, v2
	v_cvt_i32_f32_e32 v26, v2
	v_or_b32_e32 v2, 0x600, v0
	v_lshrrev_b32_e32 v30, 5, v2
	v_lshlrev_b32_e32 v2, 11, v30
	v_lshl_add_u64 v[22:23], v[4:5], 0, v[2:3]
	v_add_u32_e32 v2, s8, v30
	v_lshl_add_u64 v[24:25], v[2:3], 2, s[16:17]
	v_sub_u32_e32 v2, 0, v26
	v_med3_i32 v2, v2, -1, 3
	v_sub_u32_e32 v2, 0, v2
	global_load_dword v38, v[24:25], off
	v_ldexp_f32 v2, s4, v2
	s_waitcnt vmcnt(6)
	v_pk_mul_f32 v[10:11], v[10:11], v[2:3] op_sel_hi:[1,0]
	v_pk_mul_f32 v[26:27], v[12:13], v[2:3] op_sel_hi:[1,0]
	s_waitcnt vmcnt(5)
	v_mul_f32_e32 v2, v41, v41
	v_mul_f32_e32 v2, v37, v2
	v_max_f32_e32 v2, 0x2b8cbccc, v2
	v_cmp_gt_f32_e32 vcc, s5, v2
	v_cvt_pk_f16_f32 v24, v10, v11
	global_load_dwordx4 v[14:17], v[16:17], off
	v_cndmask_b32_e64 v10, 0, 32, vcc
	v_ldexp_f32 v2, v2, v10
	v_log_f32_e32 v25, v2
	v_or_b32_e32 v2, 0x700, v0
	v_lshrrev_b32_e32 v39, 5, v2
	v_lshlrev_b32_e32 v2, 11, v39
	v_lshl_add_u64 v[4:5], v[4:5], 0, v[2:3]
	v_add_u32_e32 v2, s8, v39
	global_load_dwordx4 v[10:13], v[22:23], off
	v_lshl_add_u64 v[22:23], v[2:3], 2, s[16:17]
	global_load_dword v40, v[22:23], off
	v_cndmask_b32_e32 v2, 0, v32, vcc
	v_sub_f32_e32 v2, v25, v2
	v_cvt_pk_f16_f32 v25, v26, v27
	v_mad_u32_u24 v22, v33, s0, v35
	ds_write_b64 v22, v[24:25]
	v_mul_f32_e32 v2, 0.5, v2
	v_rndne_f32_e32 v2, v2
	v_cvt_i32_f32_e32 v2, v2
	v_sub_u32_e32 v2, 0, v2
	s_waitcnt vmcnt(6)
	v_mul_f32_e32 v22, v29, v29
	v_mul_f32_e32 v22, v37, v22
	v_max_f32_e32 v22, 0x2b8cbccc, v22
	v_cmp_gt_f32_e32 vcc, s5, v22
	v_med3_i32 v2, v2, -1, 3
	v_sub_u32_e32 v2, 0, v2
	v_cndmask_b32_e64 v23, 0, 32, vcc
	v_ldexp_f32 v22, v22, v23
	v_log_f32_e32 v26, v22
	global_load_dwordx4 v[22:25], v[4:5], off
	v_ldexp_f32 v2, s4, v2
	v_pk_mul_f32 v[18:19], v[18:19], v[2:3] op_sel_hi:[1,0]
	s_nop 0
	v_cvt_pk_f16_f32 v4, v18, v19
	v_pk_mul_f32 v[18:19], v[20:21], v[2:3] op_sel_hi:[1,0]
	v_cndmask_b32_e32 v2, 0, v32, vcc
	v_sub_f32_e32 v2, v26, v2
	v_mul_f32_e32 v2, 0.5, v2
	v_rndne_f32_e32 v2, v2
	v_cvt_pk_f16_f32 v5, v18, v19
	v_mad_u32_u24 v18, v36, s0, v35
	v_cvt_i32_f32_e32 v2, v2
	ds_write_b64 v18, v[4:5]
	s_waitcnt vmcnt(6)
	v_mul_f32_e32 v4, v34, v34
	v_mul_f32_e32 v4, v37, v4
	v_max_f32_e32 v4, 0x2b8cbccc, v4
	v_cmp_gt_f32_e32 vcc, s5, v4
	v_sub_u32_e32 v2, 0, v2
	v_med3_i32 v2, v2, -1, 3
	v_cndmask_b32_e64 v5, 0, 32, vcc
	v_ldexp_f32 v4, v4, v5
	v_sub_u32_e32 v2, 0, v2
	v_log_f32_e32 v18, v4
	v_ldexp_f32 v2, s4, v2
	s_waitcnt vmcnt(5)
	v_pk_mul_f32 v[4:5], v[6:7], v[2:3] op_sel_hi:[1,0]
	v_pk_mul_f32 v[6:7], v[8:9], v[2:3] op_sel_hi:[1,0]
	v_cvt_pk_f16_f32 v4, v4, v5
	v_cndmask_b32_e32 v5, 0, v32, vcc
	v_sub_f32_e32 v5, v18, v5
	v_mul_f32_e32 v5, 0.5, v5
	v_rndne_f32_e32 v5, v5
	v_cvt_i32_f32_e32 v18, v5
	v_cvt_pk_f16_f32 v5, v6, v7
	ds_write_b64 v28, v[4:5] offset:8704
	s_waitcnt vmcnt(4)
	v_mul_f32_e32 v6, v38, v38
	v_mul_f32_e32 v6, v37, v6
	v_max_f32_e32 v6, 0x2b8cbccc, v6
	v_cmp_gt_f32_e32 vcc, s5, v6
	v_sub_u32_e32 v2, 0, v18
	v_med3_i32 v2, v2, -1, 3
	v_cndmask_b32_e64 v7, 0, 32, vcc
	v_ldexp_f32 v6, v6, v7
	v_log_f32_e32 v8, v6
	v_sub_u32_e32 v2, 0, v2
	v_ldexp_f32 v2, s4, v2
	s_waitcnt vmcnt(3)
	v_pk_mul_f32 v[4:5], v[14:15], v[2:3] op_sel_hi:[1,0]
	v_pk_mul_f32 v[6:7], v[16:17], v[2:3] op_sel_hi:[1,0]
	v_cndmask_b32_e32 v2, 0, v32, vcc
	v_sub_f32_e32 v2, v8, v2
	v_cvt_pk_f16_f32 v4, v4, v5
	v_mul_f32_e32 v2, 0.5, v2
	v_cvt_pk_f16_f32 v5, v6, v7
	v_mad_u32_u24 v6, v31, s0, v35
	v_rndne_f32_e32 v2, v2
	ds_write_b64 v6, v[4:5]
	s_waitcnt vmcnt(1)
	v_mul_f32_e32 v6, v40, v40
	v_cvt_i32_f32_e32 v2, v2
	v_mul_f32_e32 v6, v37, v6
	v_max_f32_e32 v6, 0x2b8cbccc, v6
	v_cmp_gt_f32_e32 vcc, s5, v6
	v_sub_u32_e32 v2, 0, v2
	v_med3_i32 v2, v2, -1, 3
	v_cndmask_b32_e64 v7, 0, 32, vcc
	v_ldexp_f32 v6, v6, v7
	v_log_f32_e32 v8, v6
	v_sub_u32_e32 v2, 0, v2
	v_ldexp_f32 v2, s4, v2
	v_pk_mul_f32 v[4:5], v[10:11], v[2:3] op_sel_hi:[1,0]
	v_pk_mul_f32 v[6:7], v[12:13], v[2:3] op_sel_hi:[1,0]
	v_cndmask_b32_e32 v2, 0, v32, vcc
	v_sub_f32_e32 v2, v8, v2
	v_mul_f32_e32 v2, 0.5, v2
	v_rndne_f32_e32 v2, v2
	v_cvt_i32_f32_e32 v2, v2
	v_cvt_pk_f16_f32 v4, v4, v5
	v_cvt_pk_f16_f32 v5, v6, v7
	v_mad_u32_u24 v6, v30, s0, v35
	v_sub_u32_e32 v2, 0, v2
	v_med3_i32 v2, v2, -1, 3
	v_sub_u32_e32 v2, 0, v2
	v_ldexp_f32 v2, s4, v2
	ds_write_b64 v6, v[4:5]
	s_waitcnt vmcnt(0)
	v_pk_mul_f32 v[4:5], v[22:23], v[2:3] op_sel_hi:[1,0]
	v_pk_mul_f32 v[6:7], v[24:25], v[2:3] op_sel_hi:[1,0]
	v_cvt_pk_f16_f32 v4, v4, v5
	v_cvt_pk_f16_f32 v5, v6, v7
	v_mad_u32_u24 v2, v39, s0, v35
	ds_write_b64 v2, v[4:5]
	v_lshrrev_b32_e32 v2, 6, v0
	v_and_b32_e32 v4, 15, v0
	v_lshl_or_b32 v4, v2, 4, v4
	v_and_b32_e32 v0, 48, v0
	v_lshrrev_b32_e32 v0, 1, v0
	v_mad_u32_u24 v12, v4, s0, v0
	s_lshl_b32 s0, s2, 12
	s_add_u32 s0, s6, s0
	s_addc_u32 s1, s7, 0
	v_lshlrev_b32_e32 v2, 10, v2
	v_lshl_add_u64 v[4:5], s[0:1], 0, v[2:3]
	v_lshlrev_b32_e32 v2, 4, v1
	s_waitcnt lgkmcnt(0)
	s_barrier
	v_lshl_add_u64 v[8:9], v[4:5], 0, v[2:3]
	ds_read_b64 v[0:1], v12
	ds_read_b64 v[2:3], v12 offset:32
	ds_read_b64 v[4:5], v12 offset:64
	ds_read_b64 v[6:7], v12 offset:96
	s_lshl_b32 s0, s3, 19
	s_lshl_b32 s1, s10, 17
	s_or_b32 s8, s0, s1
	v_lshl_add_u64 v[10:11], v[8:9], 0, s[8:9]
	s_or_b32 s0, s8, 0x8000
	s_mov_b32 s1, s9
	s_waitcnt lgkmcnt(2)
	global_store_dwordx4 v[10:11], v[0:3], off
	s_nop 1
	v_lshl_add_u64 v[0:1], v[8:9], 0, s[0:1]
	s_waitcnt lgkmcnt(0)
	global_store_dwordx4 v[0:1], v[4:7], off
	ds_read_b64 v[0:1], v12 offset:128
	ds_read_b64 v[2:3], v12 offset:160
	ds_read_b64 v[4:5], v12 offset:192
	ds_read_b64 v[6:7], v12 offset:224
	s_or_b32 s0, s8, 0x10000
	v_lshl_add_u64 v[10:11], v[8:9], 0, s[0:1]
	s_or_b32 s8, s8, 0x18000
	s_waitcnt lgkmcnt(2)
	global_store_dwordx4 v[10:11], v[0:3], off
	s_nop 1
	v_lshl_add_u64 v[0:1], v[8:9], 0, s[8:9]
	s_waitcnt lgkmcnt(0)
	global_store_dwordx4 v[0:1], v[4:7], off
	s_endpgm

.LBB1_2:
	v_lshrrev_b32_e32 v151, 4, v137
	s_lshl_b64 s[6:7], s[2:3], 4
	v_cmp_eq_u32_e64 s[2:3], 1, v151
	s_waitcnt vmcnt(31)
	v_cvt_f16_f32_e32 v8, v8
	v_cmp_gt_u32_e32 vcc, 16, v137
	s_waitcnt vmcnt(29)
	v_cndmask_b32_e64 v116, 0, v116, s[2:3]
	s_waitcnt vmcnt(21)
	v_cndmask_b32_e64 v100, 0, v100, s[2:3]
	v_cmp_eq_u32_e64 s[0:1], 2, v151
	v_cndmask_b32_e64 v114, 0, v114, s[2:3]
	v_cndmask_b32_e64 v115, 0, v115, s[2:3]
	v_cndmask_b32_e32 v6, v116, v6, vcc
	v_cndmask_b32_e64 v116, 0, v117, s[2:3]
	v_cndmask_b32_e64 v108, 0, v108, s[2:3]
	v_cndmask_b32_e32 v26, v100, v26, vcc
	v_cvt_f16_f32_e32 v29, v29
	v_cndmask_b32_e64 v100, 0, v101, s[2:3]
	v_cndmask_b32_e32 v28, 0, v28, vcc
	v_cndmask_b32_e64 v152, 0, 1.0, s[0:1]
	v_cndmask_b32_e32 v114, v114, v120, vcc
	v_cndmask_b32_e32 v115, v115, v121, vcc
	v_cndmask_b32_e32 v7, v116, v7, vcc
	v_cndmask_b32_e64 v106, 0, v106, s[2:3]
	v_cndmask_b32_e64 v107, 0, v107, s[2:3]
	v_cndmask_b32_e32 v14, v108, v14, vcc
	v_cndmask_b32_e64 v108, 0, v109, s[2:3]
	v_cndmask_b32_e32 v27, v100, v27, vcc
	v_cvt_f16_f32_e32 v100, v28
	v_cndmask_b32_e32 v116, 0, v8, vcc
	v_cvt_pk_f16_f32 v8, v6, v7
	v_cvt_pk_f16_f32 v7, v114, v115
	v_cndmask_b32_e64 v114, v152, v140, s[2:3]
	v_cndmask_b32_e32 v106, v106, v112, vcc
	v_cndmask_b32_e32 v107, v107, v113, vcc
	v_cndmask_b32_e32 v15, v108, v15, vcc
	v_cndmask_b32_e64 v98, 0, v98, s[2:3]
	v_cndmask_b32_e64 v99, 0, v99, s[2:3]
	v_cndmask_b32_e32 v110, v114, v110, vcc
	v_cndmask_b32_e64 v114, 0, v141, s[2:3]
	v_cndmask_b32_e32 v108, 0, v16, vcc
	v_cvt_pk_f16_f32 v16, v14, v15
	v_cvt_pk_f16_f32 v15, v106, v107
	v_cndmask_b32_e64 v106, v152, v138, s[2:3]
	v_cndmask_b32_e32 v98, v98, v104, vcc
	v_cndmask_b32_e32 v99, v99, v105, vcc
	v_cndmask_b32_e32 v111, v114, v111, vcc
	v_cndmask_b32_e32 v102, v106, v102, vcc
	v_cndmask_b32_e64 v106, 0, v139, s[2:3]
	v_cndmask_b32_e32 v29, 0, v29, vcc
	v_cvt_pk_f16_f32 v28, v26, v27
	v_cvt_pk_f16_f32 v27, v98, v99
	v_lshlrev_b32_e32 v101, 10, v1
	v_bitop3_b32 v98, v151, v0, 3 bitop3:0x78
	v_lshl_add_u64 v[130:131], s[4:5], 0, v[130:131]
	v_cvt_f16_f32_e32 v4, v4
	v_cvt_pk_f16_f32 v14, v110, v111
	v_cndmask_b32_e32 v103, v106, v103, vcc
	v_pack_b32_f16 v29, v100, v29
	v_lshl_or_b32 v111, v98, 4, v101
	v_lshlrev_b32_e32 v100, 4, v1
	s_movk_i32 s4, 0xc0
	v_cndmask_b32_e64 v124, 0, v124, s[2:3]
	v_cvt_pk_f16_f32 v26, v102, v103
	v_and_b32_e32 v112, 0xc0, v100
	v_bitop3_b32 v100, v100, s4, v111 bitop3:0x26
	s_lshl_b32 s4, s20, 3
	v_lshrrev_b32_e32 v102, 5, v137
	v_lshrrev_b32_e32 v104, 1, v137
	v_cndmask_b32_e64 v122, 0, v122, s[2:3]
	v_cndmask_b32_e64 v123, 0, v123, s[2:3]
	v_cndmask_b32_e32 v2, v124, v2, vcc
	v_cvt_f16_f32_e32 v5, v5
	v_cndmask_b32_e64 v124, 0, v125, s[2:3]
	v_cvt_f16_f32_e32 v9, v9
	v_or_b32_e32 v103, s4, v102
	v_and_or_b32 v110, v104, 8, v101
	v_bitop3_b32 v101, s4, v1, v102 bitop3:0x36
	s_lshl_b32 s4, s20, 4
	v_cndmask_b32_e32 v122, v122, v128, vcc
	v_cndmask_b32_e32 v123, v123, v129, vcc
	v_cndmask_b32_e32 v3, v124, v3, vcc
	v_cndmask_b32_e32 v17, 0, v17, vcc
	v_lshlrev_b32_e32 v107, 4, v101
	v_bitop3_b32 v101, v103, v1, 2 bitop3:0x36
	s_add_i32 s4, s4, 0x10000
	v_bfe_u32 v0, v0, 4, 2
	v_cndmask_b32_e64 v144, v152, v144, s[2:3]
	v_cndmask_b32_e32 v124, 0, v4, vcc
	v_cvt_pk_f16_f32 v4, v2, v3
	v_cvt_pk_f16_f32 v3, v122, v123
	v_cndmask_b32_e64 v122, v152, v142, s[2:3]
	v_cvt_pk_f16_f32 v17, v108, v17
	s_movk_i32 s5, 0x80
	v_lshlrev_b32_e32 v108, 4, v101
	v_bitop3_b32 v101, v103, v1, 4 bitop3:0x36
	s_cmp_lt_u32 s22, 64
	v_lshlrev_b32_e32 v104, 5, v0
	v_lshlrev_b32_e32 v0, 6, v0
	v_cndmask_b32_e32 v126, v144, v126, vcc
	v_cndmask_b32_e64 v144, 0, v145, s[2:3]
	v_cndmask_b32_e32 v118, v122, v118, vcc
	v_cndmask_b32_e64 v122, 0, v143, s[2:3]
	v_bitop3_b32 v99, v112, s5, v111 bitop3:0x36
	v_lshlrev_b32_e32 v109, 4, v101
	v_bitop3_b32 v101, v103, v1, 6 bitop3:0x36
	v_lshl_or_b32 v105, s20, 8, v0
	v_mov_b32_e32 v0, 0x1ec00
	s_cselect_b64 s[4:5], -1, 0
	v_cndmask_b32_e32 v127, v144, v127, vcc
	v_cndmask_b32_e32 v5, 0, v5, vcc
	v_cndmask_b32_e32 v119, v122, v119, vcc
	v_cndmask_b32_e32 v9, 0, v9, vcc
	v_lshlrev_b32_e32 v113, 4, v101
	v_lshlrev_b32_e32 v101, 5, v1
	v_lshl_add_u32 v106, v137, 6, v0
	s_cmp_eq_u32 s20, 0
	s_cselect_b32 s31, 0, 0xffff1d00
	v_add_u32_e32 v106, s31, v106
	v_cndmask_b32_e64 v0, 0, 1, s[4:5]
	v_lshl_add_u64 v[132:133], s[8:9], 0, v[132:133]
	v_or_b32_e32 v148, 0x400, v147
	v_or_b32_e32 v149, 0x800, v147
	v_or_b32_e32 v150, 0xc00, v147
	v_cvt_pk_f16_f32 v2, v126, v127
	v_pack_b32_f16 v5, v124, v5
	v_cvt_pk_f16_f32 v6, v118, v119
	v_pack_b32_f16 v9, v116, v9
	v_bitop3_b32 v98, v112, 64, v111 bitop3:0x36
	v_lshl_or_b32 v104, s20, 7, v104
	s_mov_b32 s22, 0x98000
	s_mov_b32 s23, 0x5040100
	s_mov_b32 s24, 0x7060302
	v_add_u32_e32 v107, v107, v110
	v_add_u32_e32 v108, v108, v110
	v_add_u32_e32 v109, v109, v110
	v_add_u32_e32 v110, v113, v110
	v_add_u32_e32 v111, v112, v111
	v_lshlrev_b32_e32 v113, 4, v137
	v_or_b32_e32 v113, 0x10000, v113
	s_lshr_b32 s28, s20, 2
	s_and_b32 s29, s20, 3
	s_lshl_b32 s28, s28, 10
	s_lshl_b32 s29, s29, 2
	s_add_i32 s28, s28, s29
	v_add_u32_e32 v112, s28, v113
	v_cmp_eq_u32_e64 s[26:27], 3, v151
	v_add_u32_e32 v114, 0x12400, v101
	v_and_b32_e32 v108, 15, v137
	s_lshl_b32 s31, s20, 3
	v_add_u32_e32 v107, s31, v151
	v_xor_b32_e32 v107, v107, v108
	v_lshlrev_b32_e32 v107, 4, v107
	v_lshl_or_b32 v107, v108, 10, v107
	v_xor_b32_e32 v108, 64, v107
	v_cmp_ne_u32_e64 s[4:5], 1, v0
	s_waitcnt vmcnt(16)
	v_cndmask_b32_e64 v1, v30, v134, s[0:1]
	v_bfi_b32 v30, s10, v1, v30
	v_perm_b32 v1, v22, v134, s24
	v_cndmask_b32_e64 v22, v22, v1, s[0:1]
	v_bfi_b32 v1, s10, v135, v18
	v_perm_b32 v121, v10, v135, s24
	v_cndmask_b32_e64 v18, v18, v1, s[0:1]
	v_cndmask_b32_e64 v10, v10, v121, s[0:1]
	v_mov_b32_e32 v121, v136
	v_mov_b32_e32 v144, v136
	v_mov_b32_e32 v145, v136
	v_mov_b32_e32 v0, v136
	v_mov_b32_e32 v1, v136
	s_waitcnt lgkmcnt(0)
	s_barrier
	ds_read_u16 v102, v114
	ds_read_u16 v103, v114 offset:512
	ds_read_u16 v115, v114 offset:1024
	ds_read_u16 v116, v114 offset:1536
	v_add_u32_e32 v0, 0x12c00, v105
	ds_read_b128 v[240:243], v0
	ds_read_b128 v[244:247], v0 offset:16
	ds_read_b128 v[248:251], v0 offset:32
	ds_read_b128 v[252:255], v0 offset:48
	v_add_u32_e32 v114, 2, v114
	s_branch .LBB1_4

.LBB1_4:
	s_waitcnt lgkmcnt(0)
	s_and_saveexec_b64 s[8:9], s[2:3]
	v_perm_b32 v5, v1, v102, s23
	v_perm_b32 v9, v121, v103, s23
	v_perm_b32 v17, v144, v115, s23
	v_perm_b32 v29, v145, v116, s23
	s_or_b64 exec, exec, s[8:9]
	v_mfma_f32_16x16x32_f16 v[152:155], v[30:33], v[2:5], 0
	v_mfma_f32_16x16x32_f16 v[168:171], v[22:25], v[2:5], 0
	s_cmp_lg_u32 s22, 0x818000
	v_mfma_f32_16x16x32_f16 v[156:159], v[30:33], v[6:9], 0
	v_mfma_f32_16x16x32_f16 v[172:175], v[22:25], v[6:9], 0
	s_cselect_b32 s9, s11, 15
	v_mfma_f32_16x16x32_f16 v[160:163], v[30:33], v[14:17], 0
	v_mfma_f32_16x16x32_f16 v[176:179], v[22:25], v[14:17], 0
	v_mfma_f32_16x16x32_f16 v[164:167], v[30:33], v[26:29], 0
	v_mfma_f32_16x16x32_f16 v[180:183], v[22:25], v[26:29], 0
	v_mfma_f32_16x16x32_f16 v[184:187], v[18:21], v[2:5], 0
	v_cvt_pk_f16_f32 v216, v152, v153
	v_cvt_pk_f16_f32 v217, v154, v155
	v_pk_max_f16 v216, v216, 0
	v_pk_max_f16 v217, v217, 0
	v_cvt_pk_f16_f32 v218, v168, v169
	v_cvt_pk_f16_f32 v219, v170, v171
	v_pk_max_f16 v218, v218, 0
	v_pk_max_f16 v219, v219, 0
	ds_write_b128 v107, v[216:219]
	v_mfma_f32_16x16x32_f16 v[200:203], v[10:13], v[2:5], 0
	v_cvt_pk_f16_f32 v220, v156, v157
	v_cvt_pk_f16_f32 v221, v158, v159
	v_pk_max_f16 v220, v220, 0
	v_pk_max_f16 v221, v221, 0
	v_cvt_pk_f16_f32 v222, v172, v173
	v_cvt_pk_f16_f32 v223, v174, v175
	v_pk_max_f16 v222, v222, 0
	v_pk_max_f16 v223, v223, 0
	ds_write_b128 v107, v[220:223] offset:16384
	v_mfma_f32_16x16x32_f16 v[188:191], v[18:21], v[6:9], 0
	v_cvt_pk_f16_f32 v224, v160, v161
	v_cvt_pk_f16_f32 v225, v162, v163
	v_pk_max_f16 v224, v224, 0
	v_pk_max_f16 v225, v225, 0
	v_cvt_pk_f16_f32 v226, v176, v177
	v_cvt_pk_f16_f32 v227, v178, v179
	v_pk_max_f16 v226, v226, 0
	v_pk_max_f16 v227, v227, 0
	ds_write_b128 v107, v[224:227] offset:32768
	v_mfma_f32_16x16x32_f16 v[204:207], v[10:13], v[6:9], 0
	v_cvt_pk_f16_f32 v228, v164, v165
	v_cvt_pk_f16_f32 v229, v166, v167
	v_pk_max_f16 v228, v228, 0
	v_pk_max_f16 v229, v229, 0
	v_cvt_pk_f16_f32 v230, v180, v181
	v_cvt_pk_f16_f32 v231, v182, v183
	v_pk_max_f16 v230, v230, 0
	v_pk_max_f16 v231, v231, 0
	ds_write_b128 v107, v[228:231] offset:49152
	v_mfma_f32_16x16x32_f16 v[192:195], v[18:21], v[14:17], 0
	v_cvt_pk_f16_f32 v232, v184, v185
	v_cvt_pk_f16_f32 v233, v186, v187
	v_pk_max_f16 v232, v232, 0
	v_pk_max_f16 v233, v233, 0
	v_cvt_pk_f16_f32 v234, v200, v201
	v_cvt_pk_f16_f32 v235, v202, v203
	v_pk_max_f16 v234, v234, 0
	v_pk_max_f16 v235, v235, 0
	ds_write_b128 v108, v[232:235]
	v_mfma_f32_16x16x32_f16 v[208:211], v[10:13], v[14:17], 0
	v_cvt_pk_f16_f32 v236, v188, v189
	v_cvt_pk_f16_f32 v237, v190, v191
	v_pk_max_f16 v236, v236, 0
	v_pk_max_f16 v237, v237, 0
	v_cvt_pk_f16_f32 v238, v204, v205
	v_cvt_pk_f16_f32 v239, v206, v207
	v_pk_max_f16 v238, v238, 0
	v_pk_max_f16 v239, v239, 0
	ds_write_b128 v108, v[236:239] offset:16384
	v_mfma_f32_16x16x32_f16 v[196:199], v[18:21], v[26:29], 0
	v_mfma_f32_16x16x32_f16 v[212:215], v[10:13], v[26:29], 0
	v_cvt_pk_f16_f32 v122, v192, v193
	v_cvt_pk_f16_f32 v123, v194, v195
	v_pk_max_f16 v122, v122, 0
	v_pk_max_f16 v123, v123, 0
	v_cvt_pk_f16_f32 v124, v208, v209
	v_cvt_pk_f16_f32 v125, v210, v211
	v_pk_max_f16 v124, v124, 0
	v_pk_max_f16 v125, v125, 0
	ds_write_b128 v108, v[122:125] offset:32768
	v_cvt_pk_f16_f32 v126, v196, v197
	v_cvt_pk_f16_f32 v127, v198, v199
	v_pk_max_f16 v126, v126, 0
	v_pk_max_f16 v127, v127, 0
	v_cvt_pk_f16_f32 v128, v212, v213
	v_cvt_pk_f16_f32 v129, v214, v215
	v_pk_max_f16 v128, v128, 0
	v_pk_max_f16 v129, v129, 0
	ds_write_b128 v108, v[126:129] offset:49152
	s_waitcnt lgkmcnt(0)
	s_barrier
	ds_read_b128 v[122:125], v111
	ds_read_b128 v[126:129], v111 offset:16384
	ds_read_b128 v[134:137], v111 offset:32768
	ds_read_b128 v[138:141], v111 offset:49152
	ds_read_b128 v[142:145], v98
	ds_read_b128 v[152:155], v98 offset:16384
	ds_read_b128 v[156:159], v98 offset:32768
	ds_read_b128 v[160:163], v98 offset:49152
	s_lshl_b32 s20, s9, 7
	v_lshl_add_u64 v[0:1], s[20:21], 3, v[132:133]
	s_add_i32 s25, s22, 0xfff88000
	s_lshl_b32 s8, s9, 8
	buffer_load_dwordx4 v[192:195], v147, s[16:19], s25 offen
	buffer_load_dwordx4 v[196:199], v148, s[16:19], s25 offen
	buffer_load_dwordx4 v[200:203], v149, s[16:19], s25 offen
	buffer_load_dwordx4 v[204:207], v150, s[16:19], s25 offen
	s_waitcnt vmcnt(19) lgkmcnt(7)
	v_mfma_f32_16x16x32_f16 v[164:167], v[58:61], v[122:125], v[240:243]
	s_waitcnt lgkmcnt(6)
	v_mfma_f32_16x16x32_f16 v[168:171], v[58:61], v[126:129], v[240:243]
	s_waitcnt lgkmcnt(5)
	v_mfma_f32_16x16x32_f16 v[172:175], v[58:61], v[134:137], v[240:243]
	s_waitcnt lgkmcnt(4)
	v_mfma_f32_16x16x32_f16 v[10:13], v[58:61], v[138:141], v[240:243]
	s_waitcnt vmcnt(18)
	v_mfma_f32_16x16x32_f16 v[58:61], v[54:57], v[122:125], v[244:247]
	v_mfma_f32_16x16x32_f16 v[176:179], v[54:57], v[126:129], v[244:247]
	v_mfma_f32_16x16x32_f16 v[180:183], v[54:57], v[134:137], v[244:247]
	v_mfma_f32_16x16x32_f16 v[18:21], v[54:57], v[138:141], v[244:247]
	s_waitcnt vmcnt(17)
	v_mfma_f32_16x16x32_f16 v[54:57], v[50:53], v[122:125], v[248:251]
	v_mfma_f32_16x16x32_f16 v[184:187], v[50:53], v[126:129], v[248:251]
	v_mfma_f32_16x16x32_f16 v[188:191], v[50:53], v[134:137], v[248:251]
	v_mfma_f32_16x16x32_f16 v[22:25], v[50:53], v[138:141], v[248:251]
	s_waitcnt vmcnt(16)
	v_mfma_f32_16x16x32_f16 v[50:53], v[38:41], v[122:125], v[252:255]
	v_mfma_f32_16x16x32_f16 v[122:125], v[38:41], v[126:129], v[252:255]
	v_mfma_f32_16x16x32_f16 v[126:129], v[38:41], v[134:137], v[252:255]
	v_mfma_f32_16x16x32_f16 v[38:41], v[38:41], v[138:141], v[252:255]
	ds_read_b128 v[136:139], v99
	ds_read_b128 v[208:211], v99 offset:16384
	ds_read_b128 v[212:215], v99 offset:32768
	ds_read_b128 v[216:219], v99 offset:49152
	s_add_i32 s9, s22, 0xfff90000
	s_waitcnt vmcnt(15) lgkmcnt(7)
	v_mfma_f32_16x16x32_f16 v[164:167], v[94:97], v[142:145], v[164:167]
	s_waitcnt lgkmcnt(6)
	v_mfma_f32_16x16x32_f16 v[168:171], v[94:97], v[152:155], v[168:171]
	s_waitcnt vmcnt(14)
	v_mfma_f32_16x16x32_f16 v[58:61], v[90:93], v[142:145], v[58:61]
	v_mfma_f32_16x16x32_f16 v[176:179], v[90:93], v[152:155], v[176:179]
	s_waitcnt vmcnt(13)
	v_mfma_f32_16x16x32_f16 v[54:57], v[78:81], v[142:145], v[54:57]
	v_mfma_f32_16x16x32_f16 v[184:187], v[78:81], v[152:155], v[184:187]
	s_waitcnt vmcnt(12)
	v_mfma_f32_16x16x32_f16 v[50:53], v[34:37], v[142:145], v[50:53]
	buffer_load_dwordx4 v[140:143], v147, s[16:19], s9 offen
	buffer_load_dwordx4 v[220:223], v148, s[16:19], s9 offen
	v_mfma_f32_16x16x32_f16 v[122:125], v[34:37], v[152:155], v[122:125]
	buffer_load_dwordx4 v[152:155], v149, s[16:19], s9 offen
	buffer_load_dwordx4 v[224:227], v150, s[16:19], s9 offen
	s_mov_b32 s9, s21
	s_waitcnt lgkmcnt(5)
	v_mfma_f32_16x16x32_f16 v[172:175], v[94:97], v[156:159], v[172:175]
	s_waitcnt lgkmcnt(4)
	v_mfma_f32_16x16x32_f16 v[94:97], v[94:97], v[160:163], v[10:13]
	s_nop 2
	v_lshl_add_u64 v[10:11], s[8:9], 4, v[130:131]
	v_mfma_f32_16x16x32_f16 v[180:183], v[90:93], v[156:159], v[180:183]
	v_mfma_f32_16x16x32_f16 v[90:93], v[90:93], v[160:163], v[18:21]
	v_mfma_f32_16x16x32_f16 v[188:191], v[78:81], v[156:159], v[188:191]
	v_mfma_f32_16x16x32_f16 v[78:81], v[78:81], v[160:163], v[22:25]
	global_load_dwordx4 v[30:33], v[10:11], off
	s_nop 1
	global_load_dwordx4 v[22:25], v[10:11], off offset:1024
	global_load_dwordx4 v[18:21], v[10:11], off offset:2048
	s_nop 0
	global_load_dwordx4 v[10:13], v[10:11], off offset:3072
	s_nop 0
	global_load_dwordx2 v[134:135], v[0:1], off
	v_mfma_f32_16x16x32_f16 v[126:129], v[34:37], v[156:159], v[126:129]
	v_mfma_f32_16x16x32_f16 v[34:37], v[34:37], v[160:163], v[38:41]
	s_nop 2
	ds_read_b128 v[38:41], v100
	ds_read_b128 v[156:159], v100 offset:16384
	ds_read_b128 v[160:163], v100 offset:32768
	ds_read_b128 v[228:231], v100 offset:49152
	s_add_i32 s8, s22, 0xfff98000
	s_waitcnt vmcnt(20) lgkmcnt(7)
	v_mfma_f32_16x16x32_f16 v[164:167], v[82:85], v[136:139], v[164:167]
	s_waitcnt lgkmcnt(6)
	v_mfma_f32_16x16x32_f16 v[168:171], v[82:85], v[208:211], v[168:171]
	s_waitcnt lgkmcnt(5)
	v_mfma_f32_16x16x32_f16 v[172:175], v[82:85], v[212:215], v[172:175]
	s_waitcnt lgkmcnt(4)
	v_mfma_f32_16x16x32_f16 v[82:85], v[82:85], v[216:219], v[94:97]
	s_waitcnt vmcnt(19)
	v_mfma_f32_16x16x32_f16 v[58:61], v[70:73], v[136:139], v[58:61]
	v_mfma_f32_16x16x32_f16 v[94:97], v[70:73], v[208:211], v[176:179]
	v_mfma_f32_16x16x32_f16 v[176:179], v[70:73], v[212:215], v[180:183]
	v_mfma_f32_16x16x32_f16 v[70:73], v[70:73], v[216:219], v[90:93]
	s_waitcnt vmcnt(18)
	v_mfma_f32_16x16x32_f16 v[54:57], v[62:65], v[136:139], v[54:57]
	v_mfma_f32_16x16x32_f16 v[90:93], v[62:65], v[208:211], v[184:187]
	v_mfma_f32_16x16x32_f16 v[180:183], v[62:65], v[212:215], v[188:191]
	v_mfma_f32_16x16x32_f16 v[62:65], v[62:65], v[216:219], v[78:81]
	s_waitcnt vmcnt(17)
	v_mfma_f32_16x16x32_f16 v[50:53], v[42:45], v[136:139], v[50:53]
	v_mfma_f32_16x16x32_f16 v[78:81], v[42:45], v[208:211], v[122:125]
	v_mfma_f32_16x16x32_f16 v[122:125], v[42:45], v[212:215], v[126:129]
	s_nop 2
	buffer_load_dwordx4 v[126:129], v147, s[16:19], s8 offen
	buffer_load_dwordx4 v[136:139], v148, s[16:19], s8 offen
	buffer_load_dwordx4 v[184:187], v149, s[16:19], s8 offen
	buffer_load_dwordx4 v[188:191], v150, s[16:19], s8 offen
	v_mfma_f32_16x16x32_f16 v[34:37], v[42:45], v[216:219], v[34:37]
	ds_read_b128 v[42:45], v111 offset:256
	ds_read_b128 v[208:211], v111 offset:16640
	ds_read_b128 v[212:215], v111 offset:33024
	ds_read_b128 v[216:219], v111 offset:49408
	s_add_i32 s8, s22, 0xfffa0000
	s_waitcnt vmcnt(20) lgkmcnt(7)
	v_mfma_f32_16x16x32_f16 v[164:167], v[86:89], v[38:41], v[164:167]
	s_waitcnt lgkmcnt(6)
	v_mfma_f32_16x16x32_f16 v[168:171], v[86:89], v[156:159], v[168:171]
	s_waitcnt lgkmcnt(5)
	v_mfma_f32_16x16x32_f16 v[172:175], v[86:89], v[160:163], v[172:175]
	s_waitcnt lgkmcnt(4)
	v_mfma_f32_16x16x32_f16 v[82:85], v[86:89], v[228:231], v[82:85]
	s_waitcnt vmcnt(19)
	v_mfma_f32_16x16x32_f16 v[58:61], v[74:77], v[38:41], v[58:61]
	v_mfma_f32_16x16x32_f16 v[86:89], v[74:77], v[156:159], v[94:97]
	v_mfma_f32_16x16x32_f16 v[94:97], v[74:77], v[160:163], v[176:179]
	v_mfma_f32_16x16x32_f16 v[70:73], v[74:77], v[228:231], v[70:73]
	s_waitcnt vmcnt(18)
	v_mfma_f32_16x16x32_f16 v[54:57], v[66:69], v[38:41], v[54:57]
	v_mfma_f32_16x16x32_f16 v[74:77], v[66:69], v[156:159], v[90:93]
	v_mfma_f32_16x16x32_f16 v[90:93], v[66:69], v[160:163], v[180:183]
	v_mfma_f32_16x16x32_f16 v[62:65], v[66:69], v[228:231], v[62:65]
	s_waitcnt vmcnt(17)
	v_mfma_f32_16x16x32_f16 v[38:41], v[46:49], v[38:41], v[50:53]
	v_mfma_f32_16x16x32_f16 v[50:53], v[46:49], v[156:159], v[78:81]
	v_mfma_f32_16x16x32_f16 v[66:69], v[46:49], v[160:163], v[122:125]
	s_nop 1
	buffer_load_dwordx4 v[78:81], v147, s[16:19], s8 offen
	buffer_load_dwordx4 v[122:125], v148, s[16:19], s8 offen
	buffer_load_dwordx4 v[156:159], v149, s[16:19], s8 offen
	buffer_load_dwordx4 v[160:163], v150, s[16:19], s8 offen
	v_mfma_f32_16x16x32_f16 v[34:37], v[46:49], v[228:231], v[34:37]
	ds_read_b128 v[46:49], v98 offset:256
	ds_read_b128 v[176:179], v98 offset:16640
	ds_read_b128 v[180:183], v98 offset:33024
	ds_read_b128 v[228:231], v98 offset:49408
	s_add_i32 s8, s22, 0xfffa8000
	s_waitcnt vmcnt(20) lgkmcnt(7)
	v_mfma_f32_16x16x32_f16 v[164:167], v[192:195], v[42:45], v[164:167]
	s_waitcnt lgkmcnt(6)
	v_mfma_f32_16x16x32_f16 v[168:171], v[192:195], v[208:211], v[168:171]
	s_waitcnt lgkmcnt(5)
	v_mfma_f32_16x16x32_f16 v[172:175], v[192:195], v[212:215], v[172:175]
	s_waitcnt lgkmcnt(4)
	v_mfma_f32_16x16x32_f16 v[82:85], v[192:195], v[216:219], v[82:85]
	s_waitcnt vmcnt(19)
	v_mfma_f32_16x16x32_f16 v[58:61], v[196:199], v[42:45], v[58:61]
	v_mfma_f32_16x16x32_f16 v[86:89], v[196:199], v[208:211], v[86:89]
	v_mfma_f32_16x16x32_f16 v[94:97], v[196:199], v[212:215], v[94:97]
	v_mfma_f32_16x16x32_f16 v[70:73], v[196:199], v[216:219], v[70:73]
	s_waitcnt vmcnt(18)
	v_mfma_f32_16x16x32_f16 v[54:57], v[200:203], v[42:45], v[54:57]
	v_mfma_f32_16x16x32_f16 v[74:77], v[200:203], v[208:211], v[74:77]
	v_mfma_f32_16x16x32_f16 v[90:93], v[200:203], v[212:215], v[90:93]
	v_mfma_f32_16x16x32_f16 v[62:65], v[200:203], v[216:219], v[62:65]
	s_waitcnt vmcnt(17)
	v_mfma_f32_16x16x32_f16 v[38:41], v[204:207], v[42:45], v[38:41]
	v_mfma_f32_16x16x32_f16 v[42:45], v[204:207], v[208:211], v[50:53]
	v_mfma_f32_16x16x32_f16 v[50:53], v[204:207], v[212:215], v[66:69]
	s_nop 2
	buffer_load_dwordx4 v[66:69], v147, s[16:19], s8 offen
	buffer_load_dwordx4 v[192:195], v148, s[16:19], s8 offen
	buffer_load_dwordx4 v[196:199], v149, s[16:19], s8 offen
	buffer_load_dwordx4 v[200:203], v150, s[16:19], s8 offen
	v_mfma_f32_16x16x32_f16 v[34:37], v[204:207], v[216:219], v[34:37]
	ds_read_b128 v[204:207], v99 offset:256
	ds_read_b128 v[208:211], v99 offset:16640
	ds_read_b128 v[212:215], v99 offset:33024
	ds_read_b128 v[216:219], v99 offset:49408
	s_add_i32 s8, s22, 0xfffb0000
	s_waitcnt vmcnt(20) lgkmcnt(7)
	v_mfma_f32_16x16x32_f16 v[164:167], v[140:143], v[46:49], v[164:167]
	s_waitcnt lgkmcnt(6)
	v_mfma_f32_16x16x32_f16 v[168:171], v[140:143], v[176:179], v[168:171]
	s_waitcnt lgkmcnt(5)
	v_mfma_f32_16x16x32_f16 v[172:175], v[140:143], v[180:183], v[172:175]
	s_waitcnt lgkmcnt(4)
	v_mfma_f32_16x16x32_f16 v[82:85], v[140:143], v[228:231], v[82:85]
	s_waitcnt vmcnt(19)
	v_mfma_f32_16x16x32_f16 v[58:61], v[220:223], v[46:49], v[58:61]
	v_mfma_f32_16x16x32_f16 v[86:89], v[220:223], v[176:179], v[86:89]
	s_waitcnt vmcnt(18)
	v_mfma_f32_16x16x32_f16 v[54:57], v[152:155], v[46:49], v[54:57]
	v_mfma_f32_16x16x32_f16 v[74:77], v[152:155], v[176:179], v[74:77]
	v_mfma_f32_16x16x32_f16 v[90:93], v[152:155], v[180:183], v[90:93]
	v_mfma_f32_16x16x32_f16 v[62:65], v[152:155], v[228:231], v[62:65]
	s_waitcnt vmcnt(17)
	v_mfma_f32_16x16x32_f16 v[38:41], v[224:227], v[46:49], v[38:41]
	v_mfma_f32_16x16x32_f16 v[42:45], v[224:227], v[176:179], v[42:45]
	v_mfma_f32_16x16x32_f16 v[46:49], v[224:227], v[180:183], v[50:53]
	s_nop 2
	buffer_load_dwordx4 v[50:53], v147, s[16:19], s8 offen
	buffer_load_dwordx4 v[140:143], v148, s[16:19], s8 offen
	buffer_load_dwordx4 v[152:155], v149, s[16:19], s8 offen
	buffer_load_dwordx4 v[176:179], v150, s[16:19], s8 offen
	v_mfma_f32_16x16x32_f16 v[94:97], v[220:223], v[180:183], v[94:97]
	v_mfma_f32_16x16x32_f16 v[70:73], v[220:223], v[228:231], v[70:73]
	v_mfma_f32_16x16x32_f16 v[34:37], v[224:227], v[228:231], v[34:37]
	ds_read_b128 v[180:183], v100 offset:256
	ds_read_b128 v[220:223], v100 offset:16640
	ds_read_b128 v[224:227], v100 offset:33024
	ds_read_b128 v[228:231], v100 offset:49408
	s_add_i32 s8, s22, 0xfffb8000
	s_waitcnt vmcnt(15) lgkmcnt(7)
	v_mfma_f32_16x16x32_f16 v[164:167], v[126:129], v[204:207], v[164:167]
	s_waitcnt lgkmcnt(6)
	v_mfma_f32_16x16x32_f16 v[168:171], v[126:129], v[208:211], v[168:171]
	s_waitcnt lgkmcnt(5)
	v_mfma_f32_16x16x32_f16 v[172:175], v[126:129], v[212:215], v[172:175]
	s_waitcnt lgkmcnt(4)
	v_mfma_f32_16x16x32_f16 v[82:85], v[126:129], v[216:219], v[82:85]
	s_waitcnt vmcnt(14)
	v_mfma_f32_16x16x32_f16 v[58:61], v[136:139], v[204:207], v[58:61]
	v_mfma_f32_16x16x32_f16 v[86:89], v[136:139], v[208:211], v[86:89]
	v_mfma_f32_16x16x32_f16 v[94:97], v[136:139], v[212:215], v[94:97]
	v_mfma_f32_16x16x32_f16 v[70:73], v[136:139], v[216:219], v[70:73]
	s_waitcnt vmcnt(13)
	v_mfma_f32_16x16x32_f16 v[54:57], v[184:187], v[204:207], v[54:57]
	v_mfma_f32_16x16x32_f16 v[74:77], v[184:187], v[208:211], v[74:77]
	v_mfma_f32_16x16x32_f16 v[90:93], v[184:187], v[212:215], v[90:93]
	v_mfma_f32_16x16x32_f16 v[62:65], v[184:187], v[216:219], v[62:65]
	s_waitcnt vmcnt(12)
	v_mfma_f32_16x16x32_f16 v[38:41], v[188:191], v[204:207], v[38:41]
	buffer_load_dwordx4 v[126:129], v147, s[16:19], s8 offen
	buffer_load_dwordx4 v[136:139], v148, s[16:19], s8 offen
	buffer_load_dwordx4 v[184:187], v149, s[16:19], s8 offen
	buffer_load_dwordx4 v[204:207], v150, s[16:19], s8 offen
	v_mfma_f32_16x16x32_f16 v[42:45], v[188:191], v[208:211], v[42:45]
	v_mfma_f32_16x16x32_f16 v[46:49], v[188:191], v[212:215], v[46:49]
	v_mfma_f32_16x16x32_f16 v[34:37], v[188:191], v[216:219], v[34:37]
	ds_read_b128 v[188:191], v111 offset:512
	ds_read_b128 v[208:211], v111 offset:16896
	ds_read_b128 v[212:215], v111 offset:33280
	ds_read_b128 v[216:219], v111 offset:49664
	s_add_i32 s8, s22, 0xfffc0000
	s_waitcnt vmcnt(15) lgkmcnt(7)
	v_mfma_f32_16x16x32_f16 v[164:167], v[78:81], v[180:183], v[164:167]
	s_waitcnt lgkmcnt(6)
	v_mfma_f32_16x16x32_f16 v[168:171], v[78:81], v[220:223], v[168:171]
	s_waitcnt lgkmcnt(5)
	v_mfma_f32_16x16x32_f16 v[172:175], v[78:81], v[224:227], v[172:175]
	s_waitcnt lgkmcnt(4)
	v_mfma_f32_16x16x32_f16 v[78:81], v[78:81], v[228:231], v[82:85]
	s_waitcnt vmcnt(14)
	v_mfma_f32_16x16x32_f16 v[58:61], v[122:125], v[180:183], v[58:61]
	v_mfma_f32_16x16x32_f16 v[82:85], v[122:125], v[220:223], v[86:89]
	v_mfma_f32_16x16x32_f16 v[86:89], v[122:125], v[224:227], v[94:97]
	v_mfma_f32_16x16x32_f16 v[70:73], v[122:125], v[228:231], v[70:73]
	s_waitcnt vmcnt(13)
	v_mfma_f32_16x16x32_f16 v[54:57], v[156:159], v[180:183], v[54:57]
	v_mfma_f32_16x16x32_f16 v[74:77], v[156:159], v[220:223], v[74:77]
	v_mfma_f32_16x16x32_f16 v[90:93], v[156:159], v[224:227], v[90:93]
	v_mfma_f32_16x16x32_f16 v[62:65], v[156:159], v[228:231], v[62:65]
	s_waitcnt vmcnt(12)
	v_mfma_f32_16x16x32_f16 v[38:41], v[160:163], v[180:183], v[38:41]
	buffer_load_dwordx4 v[94:97], v147, s[16:19], s8 offen
	buffer_load_dwordx4 v[122:125], v148, s[16:19], s8 offen
	buffer_load_dwordx4 v[156:159], v149, s[16:19], s8 offen
	buffer_load_dwordx4 v[180:183], v150, s[16:19], s8 offen
	v_mfma_f32_16x16x32_f16 v[42:45], v[160:163], v[220:223], v[42:45]
	v_mfma_f32_16x16x32_f16 v[46:49], v[160:163], v[224:227], v[46:49]
	v_mfma_f32_16x16x32_f16 v[34:37], v[160:163], v[228:231], v[34:37]
	ds_read_b128 v[160:163], v98 offset:512
	ds_read_b128 v[220:223], v98 offset:16896
	ds_read_b128 v[224:227], v98 offset:33280
	ds_read_b128 v[228:231], v98 offset:49664
	s_add_i32 s8, s22, 0xfffc8000
	s_waitcnt vmcnt(15) lgkmcnt(7)
	v_mfma_f32_16x16x32_f16 v[164:167], v[66:69], v[188:191], v[164:167]
	s_waitcnt lgkmcnt(6)
	v_mfma_f32_16x16x32_f16 v[168:171], v[66:69], v[208:211], v[168:171]
	s_waitcnt lgkmcnt(5)
	v_mfma_f32_16x16x32_f16 v[172:175], v[66:69], v[212:215], v[172:175]
	s_waitcnt lgkmcnt(4)
	v_mfma_f32_16x16x32_f16 v[66:69], v[66:69], v[216:219], v[78:81]
	s_waitcnt vmcnt(14)
	v_mfma_f32_16x16x32_f16 v[58:61], v[192:195], v[188:191], v[58:61]
	v_mfma_f32_16x16x32_f16 v[78:81], v[192:195], v[208:211], v[82:85]
	v_mfma_f32_16x16x32_f16 v[82:85], v[192:195], v[212:215], v[86:89]
	v_mfma_f32_16x16x32_f16 v[70:73], v[192:195], v[216:219], v[70:73]
	s_waitcnt vmcnt(13)
	v_mfma_f32_16x16x32_f16 v[54:57], v[196:199], v[188:191], v[54:57]
	v_mfma_f32_16x16x32_f16 v[74:77], v[196:199], v[208:211], v[74:77]
	v_mfma_f32_16x16x32_f16 v[86:89], v[196:199], v[212:215], v[90:93]
	v_mfma_f32_16x16x32_f16 v[62:65], v[196:199], v[216:219], v[62:65]
	s_waitcnt vmcnt(12)
	v_mfma_f32_16x16x32_f16 v[38:41], v[200:203], v[188:191], v[38:41]
	buffer_load_dwordx4 v[90:93], v147, s[16:19], s8 offen
	buffer_load_dwordx4 v[188:191], v148, s[16:19], s8 offen
	buffer_load_dwordx4 v[192:195], v149, s[16:19], s8 offen
	buffer_load_dwordx4 v[196:199], v150, s[16:19], s8 offen
	v_mfma_f32_16x16x32_f16 v[42:45], v[200:203], v[208:211], v[42:45]
	v_mfma_f32_16x16x32_f16 v[46:49], v[200:203], v[212:215], v[46:49]
	v_mfma_f32_16x16x32_f16 v[34:37], v[200:203], v[216:219], v[34:37]
	ds_read_b128 v[200:203], v99 offset:512
	ds_read_b128 v[208:211], v99 offset:16896
	ds_read_b128 v[212:215], v99 offset:33280
	ds_read_b128 v[216:219], v99 offset:49664
	s_add_i32 s8, s22, 0xfffd0000
	s_waitcnt vmcnt(15) lgkmcnt(7)
	v_mfma_f32_16x16x32_f16 v[164:167], v[50:53], v[160:163], v[164:167]
	s_waitcnt lgkmcnt(6)
	v_mfma_f32_16x16x32_f16 v[168:171], v[50:53], v[220:223], v[168:171]
	s_waitcnt lgkmcnt(5)
	v_mfma_f32_16x16x32_f16 v[172:175], v[50:53], v[224:227], v[172:175]
	s_waitcnt lgkmcnt(4)
	v_mfma_f32_16x16x32_f16 v[50:53], v[50:53], v[228:231], v[66:69]
	s_waitcnt vmcnt(14)
	v_mfma_f32_16x16x32_f16 v[58:61], v[140:143], v[160:163], v[58:61]
	v_mfma_f32_16x16x32_f16 v[66:69], v[140:143], v[220:223], v[78:81]
	v_mfma_f32_16x16x32_f16 v[78:81], v[140:143], v[224:227], v[82:85]
	v_mfma_f32_16x16x32_f16 v[70:73], v[140:143], v[228:231], v[70:73]
	s_waitcnt vmcnt(13)
	v_mfma_f32_16x16x32_f16 v[54:57], v[152:155], v[160:163], v[54:57]
	v_mfma_f32_16x16x32_f16 v[74:77], v[152:155], v[220:223], v[74:77]
	v_mfma_f32_16x16x32_f16 v[82:85], v[152:155], v[224:227], v[86:89]
	v_mfma_f32_16x16x32_f16 v[62:65], v[152:155], v[228:231], v[62:65]
	s_waitcnt vmcnt(12)
	v_mfma_f32_16x16x32_f16 v[38:41], v[176:179], v[160:163], v[38:41]
	buffer_load_dwordx4 v[86:89], v147, s[16:19], s8 offen
	buffer_load_dwordx4 v[140:143], v148, s[16:19], s8 offen
	buffer_load_dwordx4 v[152:155], v149, s[16:19], s8 offen
	buffer_load_dwordx4 v[160:163], v150, s[16:19], s8 offen
	v_mfma_f32_16x16x32_f16 v[42:45], v[176:179], v[220:223], v[42:45]
	v_mfma_f32_16x16x32_f16 v[46:49], v[176:179], v[224:227], v[46:49]
	v_mfma_f32_16x16x32_f16 v[34:37], v[176:179], v[228:231], v[34:37]
	ds_read_b128 v[176:179], v100 offset:512
	ds_read_b128 v[220:223], v100 offset:16896
	ds_read_b128 v[224:227], v100 offset:33280
	ds_read_b128 v[228:231], v100 offset:49664
	s_add_i32 s8, s22, 0xfffd8000
	s_waitcnt vmcnt(15) lgkmcnt(7)
	v_mfma_f32_16x16x32_f16 v[164:167], v[126:129], v[200:203], v[164:167]
	s_waitcnt lgkmcnt(6)
	v_mfma_f32_16x16x32_f16 v[168:171], v[126:129], v[208:211], v[168:171]
	s_waitcnt lgkmcnt(5)
	v_mfma_f32_16x16x32_f16 v[172:175], v[126:129], v[212:215], v[172:175]
	s_waitcnt lgkmcnt(4)
	v_mfma_f32_16x16x32_f16 v[50:53], v[126:129], v[216:219], v[50:53]
	s_waitcnt vmcnt(14)
	v_mfma_f32_16x16x32_f16 v[58:61], v[136:139], v[200:203], v[58:61]
	v_mfma_f32_16x16x32_f16 v[66:69], v[136:139], v[208:211], v[66:69]
	v_mfma_f32_16x16x32_f16 v[78:81], v[136:139], v[212:215], v[78:81]
	v_mfma_f32_16x16x32_f16 v[70:73], v[136:139], v[216:219], v[70:73]
	s_waitcnt vmcnt(13)
	v_mfma_f32_16x16x32_f16 v[54:57], v[184:187], v[200:203], v[54:57]
	v_mfma_f32_16x16x32_f16 v[74:77], v[184:187], v[208:211], v[74:77]
	v_mfma_f32_16x16x32_f16 v[82:85], v[184:187], v[212:215], v[82:85]
	v_mfma_f32_16x16x32_f16 v[62:65], v[184:187], v[216:219], v[62:65]
	s_waitcnt vmcnt(12)
	v_mfma_f32_16x16x32_f16 v[38:41], v[204:207], v[200:203], v[38:41]
	buffer_load_dwordx4 v[126:129], v147, s[16:19], s8 offen
	buffer_load_dwordx4 v[136:139], v148, s[16:19], s8 offen
	buffer_load_dwordx4 v[184:187], v149, s[16:19], s8 offen
	buffer_load_dwordx4 v[200:203], v150, s[16:19], s8 offen
	v_mfma_f32_16x16x32_f16 v[42:45], v[204:207], v[208:211], v[42:45]
	v_mfma_f32_16x16x32_f16 v[46:49], v[204:207], v[212:215], v[46:49]
	v_mfma_f32_16x16x32_f16 v[34:37], v[204:207], v[216:219], v[34:37]
	ds_read_b128 v[204:207], v111 offset:768
	ds_read_b128 v[208:211], v111 offset:17152
	ds_read_b128 v[212:215], v111 offset:33536
	ds_read_b128 v[216:219], v111 offset:49920
	s_add_i32 s8, s22, 0xfffe0000
	s_waitcnt vmcnt(15) lgkmcnt(7)
	v_mfma_f32_16x16x32_f16 v[164:167], v[94:97], v[176:179], v[164:167]
	s_waitcnt lgkmcnt(6)
	v_mfma_f32_16x16x32_f16 v[168:171], v[94:97], v[220:223], v[168:171]
	s_waitcnt vmcnt(14)
	v_mfma_f32_16x16x32_f16 v[58:61], v[122:125], v[176:179], v[58:61]
	v_mfma_f32_16x16x32_f16 v[66:69], v[122:125], v[220:223], v[66:69]
	s_waitcnt lgkmcnt(5)
	v_mfma_f32_16x16x32_f16 v[78:81], v[122:125], v[224:227], v[78:81]
	s_waitcnt lgkmcnt(4)
	v_mfma_f32_16x16x32_f16 v[70:73], v[122:125], v[228:231], v[70:73]
	s_waitcnt vmcnt(13)
	v_mfma_f32_16x16x32_f16 v[54:57], v[156:159], v[176:179], v[54:57]
	v_mfma_f32_16x16x32_f16 v[74:77], v[156:159], v[220:223], v[74:77]
	v_mfma_f32_16x16x32_f16 v[82:85], v[156:159], v[224:227], v[82:85]
	v_mfma_f32_16x16x32_f16 v[62:65], v[156:159], v[228:231], v[62:65]
	s_waitcnt vmcnt(12)
	v_mfma_f32_16x16x32_f16 v[38:41], v[180:183], v[176:179], v[38:41]
	v_mfma_f32_16x16x32_f16 v[42:45], v[180:183], v[220:223], v[42:45]
	buffer_load_dwordx4 v[122:125], v147, s[16:19], s8 offen
	buffer_load_dwordx4 v[156:159], v148, s[16:19], s8 offen
	buffer_load_dwordx4 v[176:179], v149, s[16:19], s8 offen
	buffer_load_dwordx4 v[220:223], v150, s[16:19], s8 offen
	v_mfma_f32_16x16x32_f16 v[50:53], v[94:97], v[228:231], v[50:53]
	v_mfma_f32_16x16x32_f16 v[46:49], v[180:183], v[224:227], v[46:49]
	v_mfma_f32_16x16x32_f16 v[34:37], v[180:183], v[228:231], v[34:37]
	v_mfma_f32_16x16x32_f16 v[172:175], v[94:97], v[224:227], v[172:175]
	ds_read_b128 v[94:97], v98 offset:768
	ds_read_b128 v[180:183], v98 offset:17152
	ds_read_b128 v[224:227], v98 offset:33536
	ds_read_b128 v[228:231], v98 offset:49920
	s_add_i32 s8, s22, 0xfffe8000
	s_waitcnt vmcnt(15) lgkmcnt(7)
	v_mfma_f32_16x16x32_f16 v[164:167], v[90:93], v[204:207], v[164:167]
	s_waitcnt lgkmcnt(6)
	v_mfma_f32_16x16x32_f16 v[168:171], v[90:93], v[208:211], v[168:171]
	s_waitcnt lgkmcnt(5)
	v_mfma_f32_16x16x32_f16 v[172:175], v[90:93], v[212:215], v[172:175]
	s_waitcnt lgkmcnt(4)
	v_mfma_f32_16x16x32_f16 v[90:93], v[90:93], v[216:219], v[50:53]
	s_waitcnt vmcnt(14)
	v_mfma_f32_16x16x32_f16 v[232:235], v[188:191], v[204:207], v[58:61]
	v_mfma_f32_16x16x32_f16 v[66:69], v[188:191], v[208:211], v[66:69]
	v_mfma_f32_16x16x32_f16 v[78:81], v[188:191], v[212:215], v[78:81]
	v_mfma_f32_16x16x32_f16 v[70:73], v[188:191], v[216:219], v[70:73]
	s_waitcnt vmcnt(13)
	v_mfma_f32_16x16x32_f16 v[188:191], v[192:195], v[204:207], v[54:57]
	v_mfma_f32_16x16x32_f16 v[74:77], v[192:195], v[208:211], v[74:77]
	v_mfma_f32_16x16x32_f16 v[82:85], v[192:195], v[212:215], v[82:85]
	v_mfma_f32_16x16x32_f16 v[62:65], v[192:195], v[216:219], v[62:65]
	s_waitcnt vmcnt(12)
	v_mfma_f32_16x16x32_f16 v[192:195], v[196:199], v[204:207], v[38:41]
	buffer_load_dwordx4 v[58:61], v147, s[16:19], s8 offen
	buffer_load_dwordx4 v[54:57], v148, s[16:19], s8 offen
	buffer_load_dwordx4 v[50:53], v149, s[16:19], s8 offen
	buffer_load_dwordx4 v[38:41], v150, s[16:19], s8 offen
	v_mfma_f32_16x16x32_f16 v[42:45], v[196:199], v[208:211], v[42:45]
	v_mfma_f32_16x16x32_f16 v[46:49], v[196:199], v[212:215], v[46:49]
	v_mfma_f32_16x16x32_f16 v[196:199], v[196:199], v[216:219], v[34:37]
	ds_read_b128 v[204:207], v99 offset:768
	ds_read_b128 v[208:211], v99 offset:17152
	ds_read_b128 v[212:215], v99 offset:33536
	ds_read_b128 v[216:219], v99 offset:49920
	s_add_i32 s8, s22, 0xffff0000
	s_waitcnt vmcnt(15) lgkmcnt(7)
	v_mfma_f32_16x16x32_f16 v[164:167], v[86:89], v[94:97], v[164:167]
	s_waitcnt lgkmcnt(6)
	v_mfma_f32_16x16x32_f16 v[168:171], v[86:89], v[180:183], v[168:171]
	s_waitcnt lgkmcnt(5)
	v_mfma_f32_16x16x32_f16 v[172:175], v[86:89], v[224:227], v[172:175]
	s_waitcnt lgkmcnt(4)
	v_mfma_f32_16x16x32_f16 v[86:89], v[86:89], v[228:231], v[90:93]
	s_waitcnt vmcnt(14)
	v_mfma_f32_16x16x32_f16 v[232:235], v[140:143], v[94:97], v[232:235]
	v_mfma_f32_16x16x32_f16 v[66:69], v[140:143], v[180:183], v[66:69]
	v_mfma_f32_16x16x32_f16 v[236:239], v[140:143], v[224:227], v[78:81]
	v_mfma_f32_16x16x32_f16 v[70:73], v[140:143], v[228:231], v[70:73]
	s_waitcnt vmcnt(13)
	v_mfma_f32_16x16x32_f16 v[140:143], v[152:155], v[94:97], v[188:191]
	v_mfma_f32_16x16x32_f16 v[74:77], v[152:155], v[180:183], v[74:77]
	v_mfma_f32_16x16x32_f16 v[82:85], v[152:155], v[224:227], v[82:85]
	v_mfma_f32_16x16x32_f16 v[62:65], v[152:155], v[228:231], v[62:65]
	s_waitcnt vmcnt(12)
	v_mfma_f32_16x16x32_f16 v[152:155], v[160:163], v[94:97], v[192:195]
	buffer_load_dwordx4 v[94:97], v147, s[16:19], s8 offen
	buffer_load_dwordx4 v[90:93], v148, s[16:19], s8 offen
	buffer_load_dwordx4 v[78:81], v149, s[16:19], s8 offen
	buffer_load_dwordx4 v[34:37], v150, s[16:19], s8 offen
	v_mfma_f32_16x16x32_f16 v[42:45], v[160:163], v[180:183], v[42:45]
	v_mfma_f32_16x16x32_f16 v[46:49], v[160:163], v[224:227], v[46:49]
	v_mfma_f32_16x16x32_f16 v[160:163], v[160:163], v[228:231], v[196:199]
	ds_read_b128 v[180:183], v100 offset:768
	ds_read_b128 v[188:191], v100 offset:17152
	ds_read_b128 v[192:195], v100 offset:33536
	ds_read_b128 v[196:199], v100 offset:49920
	s_add_i32 s8, s22, 0xffff8000
	s_waitcnt vmcnt(15) lgkmcnt(7)
	v_mfma_f32_16x16x32_f16 v[164:167], v[126:129], v[204:207], v[164:167]
	s_waitcnt lgkmcnt(6)
	v_mfma_f32_16x16x32_f16 v[168:171], v[126:129], v[208:211], v[168:171]
	s_waitcnt lgkmcnt(5)
	v_mfma_f32_16x16x32_f16 v[172:175], v[126:129], v[212:215], v[172:175]
	s_waitcnt lgkmcnt(4)
	v_mfma_f32_16x16x32_f16 v[86:89], v[126:129], v[216:219], v[86:89]
	s_waitcnt vmcnt(14)
	v_mfma_f32_16x16x32_f16 v[126:129], v[136:139], v[204:207], v[232:235]
	v_mfma_f32_16x16x32_f16 v[66:69], v[136:139], v[208:211], v[66:69]
	v_mfma_f32_16x16x32_f16 v[224:227], v[136:139], v[212:215], v[236:239]
	v_mfma_f32_16x16x32_f16 v[136:139], v[136:139], v[216:219], v[70:73]
	s_waitcnt vmcnt(13)
	v_mfma_f32_16x16x32_f16 v[140:143], v[184:187], v[204:207], v[140:143]
	v_mfma_f32_16x16x32_f16 v[74:77], v[184:187], v[208:211], v[74:77]
	v_mfma_f32_16x16x32_f16 v[228:231], v[184:187], v[212:215], v[82:85]
	v_mfma_f32_16x16x32_f16 v[184:187], v[184:187], v[216:219], v[62:65]
	s_waitcnt vmcnt(12)
	v_mfma_f32_16x16x32_f16 v[152:155], v[200:203], v[204:207], v[152:155]
	v_mfma_f32_16x16x32_f16 v[204:207], v[200:203], v[208:211], v[42:45]
	buffer_load_dwordx4 v[82:85], v147, s[16:19], s8 offen
	buffer_load_dwordx4 v[70:73], v148, s[16:19], s8 offen
	buffer_load_dwordx4 v[62:65], v149, s[16:19], s8 offen
	buffer_load_dwordx4 v[42:45], v150, s[16:19], s8 offen
	v_mfma_f32_16x16x32_f16 v[46:49], v[200:203], v[212:215], v[46:49]
	v_mfma_f32_16x16x32_f16 v[160:163], v[200:203], v[216:219], v[160:163]
	v_add_u32_e32 v0, 0x1ac00, v104
	ds_read_b128 v[240:243], v0
	ds_read_b128 v[244:247], v0 offset:16
	s_waitcnt vmcnt(12) lgkmcnt(5)
	v_mfma_f32_16x16x32_f16 v[164:167], v[122:125], v[180:183], v[164:167]
	v_mfma_f32_16x16x32_f16 v[126:129], v[156:159], v[180:183], v[126:129]
	v_mfma_f32_16x16x32_f16 v[140:143], v[176:179], v[180:183], v[140:143]
	v_mfma_f32_16x16x32_f16 v[152:155], v[220:223], v[180:183], v[152:155]
	s_waitcnt lgkmcnt(4)
	v_mfma_f32_16x16x32_f16 v[168:171], v[122:125], v[188:191], v[168:171]
	v_mfma_f32_16x16x32_f16 v[208:211], v[156:159], v[188:191], v[66:69]
	v_mfma_f32_16x16x32_f16 v[212:215], v[176:179], v[188:191], v[74:77]
	v_mfma_f32_16x16x32_f16 v[204:207], v[220:223], v[188:191], v[204:207]
	s_waitcnt lgkmcnt(3)
	v_mfma_f32_16x16x32_f16 v[172:175], v[122:125], v[192:195], v[172:175]
	v_cvt_pk_f16_f32 v232, v164, v165
	v_cvt_pk_f16_f32 v233, v166, v167
	v_pk_max_f16 v232, v232, 0
	v_pk_max_f16 v233, v233, 0
	v_mfma_f32_16x16x32_f16 v[224:227], v[156:159], v[192:195], v[224:227]
	v_cvt_pk_f16_f32 v234, v126, v127
	v_cvt_pk_f16_f32 v235, v128, v129
	v_pk_max_f16 v234, v234, 0
	v_pk_max_f16 v235, v235, 0
	v_mfma_f32_16x16x32_f16 v[228:231], v[176:179], v[192:195], v[228:231]
	v_cvt_pk_f16_f32 v236, v140, v141
	v_cvt_pk_f16_f32 v237, v142, v143
	v_pk_max_f16 v236, v236, 0
	v_pk_max_f16 v237, v237, 0
	v_mfma_f32_16x16x32_f16 v[216:219], v[220:223], v[192:195], v[46:49]
	v_cvt_pk_f16_f32 v238, v152, v153
	v_cvt_pk_f16_f32 v239, v154, v155
	v_pk_max_f16 v238, v238, 0
	v_pk_max_f16 v239, v239, 0
	s_waitcnt lgkmcnt(2)
	v_mfma_f32_16x16x32_f16 v[200:203], v[122:125], v[196:199], v[86:89]
	v_cvt_pk_f16_f32 v180, v168, v169
	v_cvt_pk_f16_f32 v181, v170, v171
	v_pk_max_f16 v180, v180, 0
	v_pk_max_f16 v181, v181, 0
	buffer_load_dwordx4 v[86:89], v147, s[16:19], s22 offen
	buffer_load_dwordx4 v[74:77], v148, s[16:19], s22 offen
	buffer_load_dwordx4 v[66:69], v149, s[16:19], s22 offen
	buffer_load_dwordx4 v[46:49], v150, s[16:19], s22 offen
	v_mfma_f32_16x16x32_f16 v[136:139], v[156:159], v[196:199], v[136:139]
	v_cvt_pk_f16_f32 v182, v208, v209
	v_cvt_pk_f16_f32 v183, v210, v211
	v_pk_max_f16 v182, v182, 0
	v_pk_max_f16 v183, v183, 0
	s_waitcnt lgkmcnt(1)
	v_mfma_f32_16x16x32_f16 v[252:255], v[240:243], v[232:235], 0
	v_cvt_pk_f16_f32 v232, v172, v173
	v_cvt_pk_f16_f32 v233, v174, v175
	v_pk_max_f16 v232, v232, 0
	v_pk_max_f16 v233, v233, 0
	v_mfma_f32_16x16x32_f16 v[184:187], v[176:179], v[196:199], v[184:187]
	v_cvt_pk_f16_f32 v188, v212, v213
	v_cvt_pk_f16_f32 v189, v214, v215
	v_pk_max_f16 v188, v188, 0
	v_pk_max_f16 v189, v189, 0
	s_waitcnt lgkmcnt(0)
	v_mfma_f32_16x16x32_f16 v[252:255], v[244:247], v[236:239], v[252:255]
	v_cvt_pk_f16_f32 v234, v224, v225
	v_cvt_pk_f16_f32 v235, v226, v227
	v_pk_max_f16 v234, v234, 0
	v_pk_max_f16 v235, v235, 0
	v_mfma_f32_16x16x32_f16 v[160:163], v[220:223], v[196:199], v[160:163]
	v_cvt_pk_f16_f32 v190, v204, v205
	v_cvt_pk_f16_f32 v191, v206, v207
	v_pk_max_f16 v190, v190, 0
	v_pk_max_f16 v191, v191, 0
	v_mfma_f32_16x16x32_f16 v[192:195], v[240:243], v[180:183], 0
	v_cvt_pk_f16_f32 v236, v228, v229
	v_cvt_pk_f16_f32 v237, v230, v231
	v_pk_max_f16 v236, v236, 0
	v_pk_max_f16 v237, v237, 0
	v_mfma_f32_16x16x32_f16 v[192:195], v[244:247], v[188:191], v[192:195]
	v_cvt_pk_f16_f32 v238, v216, v217
	v_cvt_pk_f16_f32 v239, v218, v219
	v_pk_max_f16 v238, v238, 0
	v_pk_max_f16 v239, v239, 0
	v_cvt_pk_f16_f32 v180, v200, v201
	v_cvt_pk_f16_f32 v181, v202, v203
	v_pk_max_f16 v180, v180, 0
	v_pk_max_f16 v181, v181, 0
	v_mfma_f32_16x16x32_f16 v[196:199], v[240:243], v[232:235], 0
	v_cvt_pk_f16_f32 v182, v136, v137
	v_cvt_pk_f16_f32 v183, v138, v139
	v_pk_max_f16 v182, v182, 0
	v_pk_max_f16 v183, v183, 0
	v_mfma_f32_16x16x32_f16 v[196:199], v[244:247], v[236:239], v[196:199]
	v_cvt_pk_f16_f32 v188, v184, v185
	v_cvt_pk_f16_f32 v189, v186, v187
	v_pk_max_f16 v188, v188, 0
	v_pk_max_f16 v189, v189, 0
	v_cvt_pk_f16_f32 v190, v160, v161
	v_cvt_pk_f16_f32 v191, v162, v163
	v_pk_max_f16 v190, v190, 0
	v_pk_max_f16 v191, v191, 0
	v_mfma_f32_16x16x32_f16 v[122:125], v[240:243], v[180:183], 0
	s_nop 0
	v_mfma_f32_16x16x32_f16 v[122:125], v[244:247], v[188:191], v[122:125]
	v_add_u32_e32 v145, 0x12c00, v105
	ds_read_b128 v[240:243], v145 offset:2048
	ds_read_b128 v[244:247], v145 offset:2064
	ds_read_b128 v[248:251], v145 offset:2080
	s_load_dword s30, s[12:13], 0x0
	v_cndmask_b32_e64 v0, v252, v192, s[2:3]
	ds_read_b128 v[252:255], v145 offset:2096
	ds_read_u16 v102, v114
	ds_read_u16 v103, v114 offset:512
	ds_read_u16 v115, v114 offset:1024
	ds_read_u16 v116, v114 offset:1536
	v_cndmask_b32_e64 v0, v0, v196, s[0:1]
	s_waitcnt vmcnt(16)
	v_cndmask_b32_e64 v1, v30, v134, s[0:1]
	v_bfi_b32 v30, s10, v1, v30
	v_perm_b32 v1, v22, v134, s24
	v_cndmask_b32_e64 v22, v22, v1, s[0:1]
	v_bfi_b32 v1, s10, v135, v18
	v_perm_b32 v121, v10, v135, s24
	v_cndmask_b32_e64 v18, v18, v1, s[0:1]
	v_cndmask_b32_e64 v10, v10, v121, s[0:1]
	v_cndmask_b32_e64 v0, v0, v122, s[26:27]
	ds_write_b32 v112, v0
	s_waitcnt lgkmcnt(0)
	s_barrier
	ds_read_b128 v[232:235], v113
	ds_read_b128 v[236:239], v113 offset:1024
	s_waitcnt lgkmcnt(0)
	v_add_f32_e32 v0, v232, v233
	v_add_f32_e32 v1, v234, v235
	v_add_f32_e32 v121, v236, v237
	v_add_f32_e32 v144, v238, v239
	v_add_f32_e32 v0, v0, v1
	v_add_f32_e32 v121, v121, v144
	v_add_f32_e32 v0, v0, v121
	v_add_f32_e32 v0, s30, v0
	ds_write_b32 v106, v0
	v_cvt_f16_f32_e32 v1, v0
	v_cvt_f16_f32_e32 v121, v0
	s_nop 1
	v_permlane16_swap_b32_e32 v1, v121
	v_mov_b32_e32 v144, v1
	v_mov_b32_e32 v145, v121
	s_nop 1
	v_permlane32_swap_b32_e32 v1, v144
	v_permlane32_swap_b32_e32 v121, v145
	s_branch .LBB1_3
